# P0 order split by vcu bit 3 (groups of 8 consecutive workgroups = full weight rows stream together) instead of bit 0
# baseline (speedup 1.0000x reference)
.Lp0_body:
	s_cmp_lg_u32 s101, 0
	s_cbranch_scc1 .Lp0_sections
	v_readlane_b32 s39, v253, 3
	s_nop 3
	s_and_b32 s2, s39, 8
	s_cbranch_scc0 .Lp0_sections
	s_mov_b32 s101, 1
	v_mbcnt_lo_u32_b32 v99, -1, 0
	v_mbcnt_hi_u32_b32 v99, -1, v99
	v_readlane_b32 s1, v253, 20
	v_readlane_b32 s78, v253, 2
	s_nop 3
	s_lshl_b32 s0, s39, 3
	s_add_i32 s16, s0, s1
	s_lshl_b32 s8, s1, 14
	s_lshl_b32 s17, s78, 3
	v_lshlrev_b32_e32 v164, 3, v99
	v_ashrrev_i32_e32 v45, 3, v99
	v_and_b32_e32 v2, 7, v99
	v_mov_b32_e32 v33, 0
	v_ashrrev_i32_e32 v38, 3, v99
	v_lshlrev_b32_e32 v32, 2, v2
	v_and_b32_e32 v44, 24, v164
	v_lshlrev_b32_e32 v131, 11, v2
	v_lshlrev_b32_e32 v34, 4, v2
	v_mov_b32_e32 v35, v33
	s_branch .LBB0_205
